# baseline (speedup 1.0000x reference)
_Z11prep_kernelPKfS0_S0_PDF16_PfPiS0_S1_:
	s_cmpk_lt_u32 s2, 0xc1
	s_mov_b64 s[4:5], -1
	s_cbranch_scc0 .LBB0_51
	s_cmpk_lg_i32 s2, 0xc0
	s_cbranch_scc0 .LBB0_11
	s_cmp_gt_u32 s2, 63
	s_cbranch_scc0 .LBB0_8
	s_load_dwordx4 s[4:7], s[0:1], 0x0
	s_load_dwordx2 s[28:29], s[0:1], 0x20
	s_lshl_b32 s3, s2, 2
	s_addk_i32 s3, 0xff00
	v_readfirstlane_b32 s23, v0
	v_lshlrev_b32_e32 v1, 2, v0
	v_and_b32_e32 v1, 0x1fc, v1
	v_lshlrev_b32_e32 v26, 2, v1
	v_mov_b32_e32 v27, 0
	s_lshr_b32 s22, s23, 7
	s_lshl_b32 s8, s3, 9
	s_lshl_b32 s9, s22, 7
	s_add_u32 s8, s8, s9
	s_lshl_b32 s10, s22, 16
	s_waitcnt lgkmcnt(0)
	s_add_u32 s20, s4, s8
	s_addc_u32 s21, s5, 0
	s_add_u32 s24, s6, s10
	s_addc_u32 s25, s7, 0
	global_load_dwordx4 v[32:35], v26, s[24:25]
	global_load_dwordx4 v[36:39], v26, s[24:25] offset:2048
	s_add_u32 s24, s24, 0x1000
	s_addc_u32 s25, s25, 0
	s_load_dwordx8 s[32:39], s[20:21], 0x0
	s_load_dwordx8 s[40:47], s[20:21], 0x200
	s_load_dwordx8 s[48:55], s[20:21], 0x400
	s_load_dwordx8 s[56:63], s[20:21], 0x600
	global_load_dwordx4 v[40:43], v26, s[24:25]
	global_load_dwordx4 v[44:47], v26, s[24:25] offset:2048
	s_add_u32 s24, s24, 0x1000
	s_addc_u32 s25, s25, 0
	s_load_dwordx8 s[64:71], s[20:21], 0x20
	s_load_dwordx8 s[72:79], s[20:21], 0x220
	s_load_dwordx8 s[80:87], s[20:21], 0x420
	s_load_dwordx8 s[88:95], s[20:21], 0x620
	global_load_dwordx4 v[48:51], v26, s[24:25]
	global_load_dwordx4 v[52:55], v26, s[24:25] offset:2048
	s_add_u32 s24, s24, 0x1000
	s_addc_u32 s25, s25, 0
	global_load_dwordx4 v[56:59], v26, s[24:25]
	global_load_dwordx4 v[60:63], v26, s[24:25] offset:2048
	s_add_u32 s24, s24, 0x1000
	s_addc_u32 s25, s25, 0
	global_load_dwordx4 v[64:67], v26, s[24:25]
	global_load_dwordx4 v[68:71], v26, s[24:25] offset:2048
	s_add_u32 s24, s24, 0x1000
	s_addc_u32 s25, s25, 0
	global_load_dwordx4 v[72:75], v26, s[24:25]
	global_load_dwordx4 v[76:79], v26, s[24:25] offset:2048
	s_add_u32 s24, s24, 0x1000
	s_addc_u32 s25, s25, 0
	global_load_dwordx4 v[80:83], v26, s[24:25]
	global_load_dwordx4 v[84:87], v26, s[24:25] offset:2048
	s_add_u32 s24, s24, 0x1000
	s_addc_u32 s25, s25, 0
	global_load_dwordx4 v[88:91], v26, s[24:25]
	global_load_dwordx4 v[92:95], v26, s[24:25] offset:2048
	s_add_u32 s24, s24, 0x1000
	s_addc_u32 s25, s25, 0
	global_load_dwordx4 v[96:99], v26, s[24:25]
	global_load_dwordx4 v[100:103], v26, s[24:25] offset:2048
	s_add_u32 s24, s24, 0x1000
	s_addc_u32 s25, s25, 0
	global_load_dwordx4 v[104:107], v26, s[24:25]
	global_load_dwordx4 v[108:111], v26, s[24:25] offset:2048
	s_add_u32 s24, s24, 0x1000
	s_addc_u32 s25, s25, 0
	global_load_dwordx4 v[112:115], v26, s[24:25]
	global_load_dwordx4 v[116:119], v26, s[24:25] offset:2048
	s_add_u32 s24, s24, 0x1000
	s_addc_u32 s25, s25, 0
	global_load_dwordx4 v[120:123], v26, s[24:25]
	global_load_dwordx4 v[124:127], v26, s[24:25] offset:2048
	s_add_u32 s24, s24, 0x1000
	s_addc_u32 s25, s25, 0
	global_load_dwordx4 v[128:131], v26, s[24:25]
	global_load_dwordx4 v[132:135], v26, s[24:25] offset:2048
	s_add_u32 s24, s24, 0x1000
	s_addc_u32 s25, s25, 0
	global_load_dwordx4 v[136:139], v26, s[24:25]
	global_load_dwordx4 v[140:143], v26, s[24:25] offset:2048
	s_add_u32 s24, s24, 0x1000
	s_addc_u32 s25, s25, 0
	global_load_dwordx4 v[144:147], v26, s[24:25]
	global_load_dwordx4 v[148:151], v26, s[24:25] offset:2048
	s_add_u32 s24, s24, 0x1000
	s_addc_u32 s25, s25, 0
	global_load_dwordx4 v[152:155], v26, s[24:25]
	global_load_dwordx4 v[156:159], v26, s[24:25] offset:2048
	v_mov_b64_e32 v[14:15], 0
	v_mov_b64_e32 v[16:17], 0
	v_mov_b64_e32 v[10:11], 0
	v_mov_b64_e32 v[12:13], 0
	v_mov_b64_e32 v[6:7], 0
	v_mov_b64_e32 v[8:9], 0
	v_mov_b64_e32 v[2:3], 0
	v_mov_b64_e32 v[4:5], 0
	s_waitcnt lgkmcnt(0)
	s_waitcnt vmcnt(31)
	v_pk_fma_f32 v[14:15], s[32:33], v[32:33], v[14:15] op_sel_hi:[0,1,1]
	v_pk_fma_f32 v[16:17], s[32:33], v[34:35], v[16:17] op_sel_hi:[0,1,1]
	v_pk_fma_f32 v[10:11], s[40:41], v[32:33], v[10:11] op_sel_hi:[0,1,1]
	v_pk_fma_f32 v[12:13], s[40:41], v[34:35], v[12:13] op_sel_hi:[0,1,1]
	v_pk_fma_f32 v[6:7], s[48:49], v[32:33], v[6:7] op_sel_hi:[0,1,1]
	v_pk_fma_f32 v[8:9], s[48:49], v[34:35], v[8:9] op_sel_hi:[0,1,1]
	v_pk_fma_f32 v[2:3], s[56:57], v[32:33], v[2:3] op_sel_hi:[0,1,1]
	v_pk_fma_f32 v[4:5], s[56:57], v[34:35], v[4:5] op_sel_hi:[0,1,1]
	s_waitcnt vmcnt(30)
	v_pk_fma_f32 v[14:15], s[32:33], v[36:37], v[14:15] op_sel:[1,0,0]
	v_pk_fma_f32 v[16:17], s[32:33], v[38:39], v[16:17] op_sel:[1,0,0]
	v_pk_fma_f32 v[10:11], s[40:41], v[36:37], v[10:11] op_sel:[1,0,0]
	v_pk_fma_f32 v[12:13], s[40:41], v[38:39], v[12:13] op_sel:[1,0,0]
	v_pk_fma_f32 v[6:7], s[48:49], v[36:37], v[6:7] op_sel:[1,0,0]
	v_pk_fma_f32 v[8:9], s[48:49], v[38:39], v[8:9] op_sel:[1,0,0]
	v_pk_fma_f32 v[2:3], s[56:57], v[36:37], v[2:3] op_sel:[1,0,0]
	v_pk_fma_f32 v[4:5], s[56:57], v[38:39], v[4:5] op_sel:[1,0,0]
	s_waitcnt vmcnt(29)
	v_pk_fma_f32 v[14:15], s[34:35], v[40:41], v[14:15] op_sel_hi:[0,1,1]
	v_pk_fma_f32 v[16:17], s[34:35], v[42:43], v[16:17] op_sel_hi:[0,1,1]
	v_pk_fma_f32 v[10:11], s[42:43], v[40:41], v[10:11] op_sel_hi:[0,1,1]
	v_pk_fma_f32 v[12:13], s[42:43], v[42:43], v[12:13] op_sel_hi:[0,1,1]
	v_pk_fma_f32 v[6:7], s[50:51], v[40:41], v[6:7] op_sel_hi:[0,1,1]
	v_pk_fma_f32 v[8:9], s[50:51], v[42:43], v[8:9] op_sel_hi:[0,1,1]
	v_pk_fma_f32 v[2:3], s[58:59], v[40:41], v[2:3] op_sel_hi:[0,1,1]
	v_pk_fma_f32 v[4:5], s[58:59], v[42:43], v[4:5] op_sel_hi:[0,1,1]
	s_waitcnt vmcnt(28)
	v_pk_fma_f32 v[14:15], s[34:35], v[44:45], v[14:15] op_sel:[1,0,0]
	v_pk_fma_f32 v[16:17], s[34:35], v[46:47], v[16:17] op_sel:[1,0,0]
	v_pk_fma_f32 v[10:11], s[42:43], v[44:45], v[10:11] op_sel:[1,0,0]
	v_pk_fma_f32 v[12:13], s[42:43], v[46:47], v[12:13] op_sel:[1,0,0]
	v_pk_fma_f32 v[6:7], s[50:51], v[44:45], v[6:7] op_sel:[1,0,0]
	v_pk_fma_f32 v[8:9], s[50:51], v[46:47], v[8:9] op_sel:[1,0,0]
	v_pk_fma_f32 v[2:3], s[58:59], v[44:45], v[2:3] op_sel:[1,0,0]
	v_pk_fma_f32 v[4:5], s[58:59], v[46:47], v[4:5] op_sel:[1,0,0]
	s_waitcnt vmcnt(27)
	v_pk_fma_f32 v[14:15], s[36:37], v[48:49], v[14:15] op_sel_hi:[0,1,1]
	v_pk_fma_f32 v[16:17], s[36:37], v[50:51], v[16:17] op_sel_hi:[0,1,1]
	v_pk_fma_f32 v[10:11], s[44:45], v[48:49], v[10:11] op_sel_hi:[0,1,1]
	v_pk_fma_f32 v[12:13], s[44:45], v[50:51], v[12:13] op_sel_hi:[0,1,1]
	v_pk_fma_f32 v[6:7], s[52:53], v[48:49], v[6:7] op_sel_hi:[0,1,1]
	v_pk_fma_f32 v[8:9], s[52:53], v[50:51], v[8:9] op_sel_hi:[0,1,1]
	v_pk_fma_f32 v[2:3], s[60:61], v[48:49], v[2:3] op_sel_hi:[0,1,1]
	v_pk_fma_f32 v[4:5], s[60:61], v[50:51], v[4:5] op_sel_hi:[0,1,1]
	s_waitcnt vmcnt(26)
	v_pk_fma_f32 v[14:15], s[36:37], v[52:53], v[14:15] op_sel:[1,0,0]
	v_pk_fma_f32 v[16:17], s[36:37], v[54:55], v[16:17] op_sel:[1,0,0]
	v_pk_fma_f32 v[10:11], s[44:45], v[52:53], v[10:11] op_sel:[1,0,0]
	v_pk_fma_f32 v[12:13], s[44:45], v[54:55], v[12:13] op_sel:[1,0,0]
	v_pk_fma_f32 v[6:7], s[52:53], v[52:53], v[6:7] op_sel:[1,0,0]
	v_pk_fma_f32 v[8:9], s[52:53], v[54:55], v[8:9] op_sel:[1,0,0]
	v_pk_fma_f32 v[2:3], s[60:61], v[52:53], v[2:3] op_sel:[1,0,0]
	v_pk_fma_f32 v[4:5], s[60:61], v[54:55], v[4:5] op_sel:[1,0,0]
	s_waitcnt vmcnt(25)
	v_pk_fma_f32 v[14:15], s[38:39], v[56:57], v[14:15] op_sel_hi:[0,1,1]
	v_pk_fma_f32 v[16:17], s[38:39], v[58:59], v[16:17] op_sel_hi:[0,1,1]
	v_pk_fma_f32 v[10:11], s[46:47], v[56:57], v[10:11] op_sel_hi:[0,1,1]
	v_pk_fma_f32 v[12:13], s[46:47], v[58:59], v[12:13] op_sel_hi:[0,1,1]
	v_pk_fma_f32 v[6:7], s[54:55], v[56:57], v[6:7] op_sel_hi:[0,1,1]
	v_pk_fma_f32 v[8:9], s[54:55], v[58:59], v[8:9] op_sel_hi:[0,1,1]
	v_pk_fma_f32 v[2:3], s[62:63], v[56:57], v[2:3] op_sel_hi:[0,1,1]
	v_pk_fma_f32 v[4:5], s[62:63], v[58:59], v[4:5] op_sel_hi:[0,1,1]
	s_waitcnt vmcnt(24)
	v_pk_fma_f32 v[14:15], s[38:39], v[60:61], v[14:15] op_sel:[1,0,0]
	v_pk_fma_f32 v[16:17], s[38:39], v[62:63], v[16:17] op_sel:[1,0,0]
	v_pk_fma_f32 v[10:11], s[46:47], v[60:61], v[10:11] op_sel:[1,0,0]
	v_pk_fma_f32 v[12:13], s[46:47], v[62:63], v[12:13] op_sel:[1,0,0]
	v_pk_fma_f32 v[6:7], s[54:55], v[60:61], v[6:7] op_sel:[1,0,0]
	v_pk_fma_f32 v[8:9], s[54:55], v[62:63], v[8:9] op_sel:[1,0,0]
	v_pk_fma_f32 v[2:3], s[62:63], v[60:61], v[2:3] op_sel:[1,0,0]
	v_pk_fma_f32 v[4:5], s[62:63], v[62:63], v[4:5] op_sel:[1,0,0]
	s_load_dwordx8 s[32:39], s[20:21], 0x40
	s_load_dwordx8 s[40:47], s[20:21], 0x240
	s_load_dwordx8 s[48:55], s[20:21], 0x440
	s_load_dwordx8 s[56:63], s[20:21], 0x640
	s_waitcnt vmcnt(23)
	v_pk_fma_f32 v[14:15], s[64:65], v[64:65], v[14:15] op_sel_hi:[0,1,1]
	v_pk_fma_f32 v[16:17], s[64:65], v[66:67], v[16:17] op_sel_hi:[0,1,1]
	v_pk_fma_f32 v[10:11], s[72:73], v[64:65], v[10:11] op_sel_hi:[0,1,1]
	v_pk_fma_f32 v[12:13], s[72:73], v[66:67], v[12:13] op_sel_hi:[0,1,1]
	v_pk_fma_f32 v[6:7], s[80:81], v[64:65], v[6:7] op_sel_hi:[0,1,1]
	v_pk_fma_f32 v[8:9], s[80:81], v[66:67], v[8:9] op_sel_hi:[0,1,1]
	v_pk_fma_f32 v[2:3], s[88:89], v[64:65], v[2:3] op_sel_hi:[0,1,1]
	v_pk_fma_f32 v[4:5], s[88:89], v[66:67], v[4:5] op_sel_hi:[0,1,1]
	s_waitcnt vmcnt(22)
	v_pk_fma_f32 v[14:15], s[64:65], v[68:69], v[14:15] op_sel:[1,0,0]
	v_pk_fma_f32 v[16:17], s[64:65], v[70:71], v[16:17] op_sel:[1,0,0]
	v_pk_fma_f32 v[10:11], s[72:73], v[68:69], v[10:11] op_sel:[1,0,0]
	v_pk_fma_f32 v[12:13], s[72:73], v[70:71], v[12:13] op_sel:[1,0,0]
	v_pk_fma_f32 v[6:7], s[80:81], v[68:69], v[6:7] op_sel:[1,0,0]
	v_pk_fma_f32 v[8:9], s[80:81], v[70:71], v[8:9] op_sel:[1,0,0]
	v_pk_fma_f32 v[2:3], s[88:89], v[68:69], v[2:3] op_sel:[1,0,0]
	v_pk_fma_f32 v[4:5], s[88:89], v[70:71], v[4:5] op_sel:[1,0,0]
	s_waitcnt vmcnt(21)
	v_pk_fma_f32 v[14:15], s[66:67], v[72:73], v[14:15] op_sel_hi:[0,1,1]
	v_pk_fma_f32 v[16:17], s[66:67], v[74:75], v[16:17] op_sel_hi:[0,1,1]
	v_pk_fma_f32 v[10:11], s[74:75], v[72:73], v[10:11] op_sel_hi:[0,1,1]
	v_pk_fma_f32 v[12:13], s[74:75], v[74:75], v[12:13] op_sel_hi:[0,1,1]
	v_pk_fma_f32 v[6:7], s[82:83], v[72:73], v[6:7] op_sel_hi:[0,1,1]
	v_pk_fma_f32 v[8:9], s[82:83], v[74:75], v[8:9] op_sel_hi:[0,1,1]
	v_pk_fma_f32 v[2:3], s[90:91], v[72:73], v[2:3] op_sel_hi:[0,1,1]
	v_pk_fma_f32 v[4:5], s[90:91], v[74:75], v[4:5] op_sel_hi:[0,1,1]
	s_waitcnt vmcnt(20)
	v_pk_fma_f32 v[14:15], s[66:67], v[76:77], v[14:15] op_sel:[1,0,0]
	v_pk_fma_f32 v[16:17], s[66:67], v[78:79], v[16:17] op_sel:[1,0,0]
	v_pk_fma_f32 v[10:11], s[74:75], v[76:77], v[10:11] op_sel:[1,0,0]
	v_pk_fma_f32 v[12:13], s[74:75], v[78:79], v[12:13] op_sel:[1,0,0]
	v_pk_fma_f32 v[6:7], s[82:83], v[76:77], v[6:7] op_sel:[1,0,0]
	v_pk_fma_f32 v[8:9], s[82:83], v[78:79], v[8:9] op_sel:[1,0,0]
	v_pk_fma_f32 v[2:3], s[90:91], v[76:77], v[2:3] op_sel:[1,0,0]
	v_pk_fma_f32 v[4:5], s[90:91], v[78:79], v[4:5] op_sel:[1,0,0]
	s_waitcnt vmcnt(19)
	v_pk_fma_f32 v[14:15], s[68:69], v[80:81], v[14:15] op_sel_hi:[0,1,1]
	v_pk_fma_f32 v[16:17], s[68:69], v[82:83], v[16:17] op_sel_hi:[0,1,1]
	v_pk_fma_f32 v[10:11], s[76:77], v[80:81], v[10:11] op_sel_hi:[0,1,1]
	v_pk_fma_f32 v[12:13], s[76:77], v[82:83], v[12:13] op_sel_hi:[0,1,1]
	v_pk_fma_f32 v[6:7], s[84:85], v[80:81], v[6:7] op_sel_hi:[0,1,1]
	v_pk_fma_f32 v[8:9], s[84:85], v[82:83], v[8:9] op_sel_hi:[0,1,1]
	v_pk_fma_f32 v[2:3], s[92:93], v[80:81], v[2:3] op_sel_hi:[0,1,1]
	v_pk_fma_f32 v[4:5], s[92:93], v[82:83], v[4:5] op_sel_hi:[0,1,1]
	s_waitcnt vmcnt(18)
	v_pk_fma_f32 v[14:15], s[68:69], v[84:85], v[14:15] op_sel:[1,0,0]
	v_pk_fma_f32 v[16:17], s[68:69], v[86:87], v[16:17] op_sel:[1,0,0]
	v_pk_fma_f32 v[10:11], s[76:77], v[84:85], v[10:11] op_sel:[1,0,0]
	v_pk_fma_f32 v[12:13], s[76:77], v[86:87], v[12:13] op_sel:[1,0,0]
	v_pk_fma_f32 v[6:7], s[84:85], v[84:85], v[6:7] op_sel:[1,0,0]
	v_pk_fma_f32 v[8:9], s[84:85], v[86:87], v[8:9] op_sel:[1,0,0]
	v_pk_fma_f32 v[2:3], s[92:93], v[84:85], v[2:3] op_sel:[1,0,0]
	v_pk_fma_f32 v[4:5], s[92:93], v[86:87], v[4:5] op_sel:[1,0,0]
	s_waitcnt vmcnt(17)
	v_pk_fma_f32 v[14:15], s[70:71], v[88:89], v[14:15] op_sel_hi:[0,1,1]
	v_pk_fma_f32 v[16:17], s[70:71], v[90:91], v[16:17] op_sel_hi:[0,1,1]
	v_pk_fma_f32 v[10:11], s[78:79], v[88:89], v[10:11] op_sel_hi:[0,1,1]
	v_pk_fma_f32 v[12:13], s[78:79], v[90:91], v[12:13] op_sel_hi:[0,1,1]
	v_pk_fma_f32 v[6:7], s[86:87], v[88:89], v[6:7] op_sel_hi:[0,1,1]
	v_pk_fma_f32 v[8:9], s[86:87], v[90:91], v[8:9] op_sel_hi:[0,1,1]
	v_pk_fma_f32 v[2:3], s[94:95], v[88:89], v[2:3] op_sel_hi:[0,1,1]
	v_pk_fma_f32 v[4:5], s[94:95], v[90:91], v[4:5] op_sel_hi:[0,1,1]
	s_waitcnt vmcnt(16)
	v_pk_fma_f32 v[14:15], s[70:71], v[92:93], v[14:15] op_sel:[1,0,0]
	v_pk_fma_f32 v[16:17], s[70:71], v[94:95], v[16:17] op_sel:[1,0,0]
	v_pk_fma_f32 v[10:11], s[78:79], v[92:93], v[10:11] op_sel:[1,0,0]
	v_pk_fma_f32 v[12:13], s[78:79], v[94:95], v[12:13] op_sel:[1,0,0]
	v_pk_fma_f32 v[6:7], s[86:87], v[92:93], v[6:7] op_sel:[1,0,0]
	v_pk_fma_f32 v[8:9], s[86:87], v[94:95], v[8:9] op_sel:[1,0,0]
	v_pk_fma_f32 v[2:3], s[94:95], v[92:93], v[2:3] op_sel:[1,0,0]
	v_pk_fma_f32 v[4:5], s[94:95], v[94:95], v[4:5] op_sel:[1,0,0]
	s_waitcnt lgkmcnt(0)
	s_load_dwordx8 s[64:71], s[20:21], 0x60
	s_load_dwordx8 s[72:79], s[20:21], 0x260
	s_load_dwordx8 s[80:87], s[20:21], 0x460
	s_load_dwordx8 s[88:95], s[20:21], 0x660
	s_waitcnt vmcnt(15)
	v_pk_fma_f32 v[14:15], s[32:33], v[96:97], v[14:15] op_sel_hi:[0,1,1]
	v_pk_fma_f32 v[16:17], s[32:33], v[98:99], v[16:17] op_sel_hi:[0,1,1]
	v_pk_fma_f32 v[10:11], s[40:41], v[96:97], v[10:11] op_sel_hi:[0,1,1]
	v_pk_fma_f32 v[12:13], s[40:41], v[98:99], v[12:13] op_sel_hi:[0,1,1]
	v_pk_fma_f32 v[6:7], s[48:49], v[96:97], v[6:7] op_sel_hi:[0,1,1]
	v_pk_fma_f32 v[8:9], s[48:49], v[98:99], v[8:9] op_sel_hi:[0,1,1]
	v_pk_fma_f32 v[2:3], s[56:57], v[96:97], v[2:3] op_sel_hi:[0,1,1]
	v_pk_fma_f32 v[4:5], s[56:57], v[98:99], v[4:5] op_sel_hi:[0,1,1]
	s_waitcnt vmcnt(14)
	v_pk_fma_f32 v[14:15], s[32:33], v[100:101], v[14:15] op_sel:[1,0,0]
	v_pk_fma_f32 v[16:17], s[32:33], v[102:103], v[16:17] op_sel:[1,0,0]
	v_pk_fma_f32 v[10:11], s[40:41], v[100:101], v[10:11] op_sel:[1,0,0]
	v_pk_fma_f32 v[12:13], s[40:41], v[102:103], v[12:13] op_sel:[1,0,0]
	v_pk_fma_f32 v[6:7], s[48:49], v[100:101], v[6:7] op_sel:[1,0,0]
	v_pk_fma_f32 v[8:9], s[48:49], v[102:103], v[8:9] op_sel:[1,0,0]
	v_pk_fma_f32 v[2:3], s[56:57], v[100:101], v[2:3] op_sel:[1,0,0]
	v_pk_fma_f32 v[4:5], s[56:57], v[102:103], v[4:5] op_sel:[1,0,0]
	s_waitcnt vmcnt(13)
	v_pk_fma_f32 v[14:15], s[34:35], v[104:105], v[14:15] op_sel_hi:[0,1,1]
	v_pk_fma_f32 v[16:17], s[34:35], v[106:107], v[16:17] op_sel_hi:[0,1,1]
	v_pk_fma_f32 v[10:11], s[42:43], v[104:105], v[10:11] op_sel_hi:[0,1,1]
	v_pk_fma_f32 v[12:13], s[42:43], v[106:107], v[12:13] op_sel_hi:[0,1,1]
	v_pk_fma_f32 v[6:7], s[50:51], v[104:105], v[6:7] op_sel_hi:[0,1,1]
	v_pk_fma_f32 v[8:9], s[50:51], v[106:107], v[8:9] op_sel_hi:[0,1,1]
	v_pk_fma_f32 v[2:3], s[58:59], v[104:105], v[2:3] op_sel_hi:[0,1,1]
	v_pk_fma_f32 v[4:5], s[58:59], v[106:107], v[4:5] op_sel_hi:[0,1,1]
	s_waitcnt vmcnt(12)
	v_pk_fma_f32 v[14:15], s[34:35], v[108:109], v[14:15] op_sel:[1,0,0]
	v_pk_fma_f32 v[16:17], s[34:35], v[110:111], v[16:17] op_sel:[1,0,0]
	v_pk_fma_f32 v[10:11], s[42:43], v[108:109], v[10:11] op_sel:[1,0,0]
	v_pk_fma_f32 v[12:13], s[42:43], v[110:111], v[12:13] op_sel:[1,0,0]
	v_pk_fma_f32 v[6:7], s[50:51], v[108:109], v[6:7] op_sel:[1,0,0]
	v_pk_fma_f32 v[8:9], s[50:51], v[110:111], v[8:9] op_sel:[1,0,0]
	v_pk_fma_f32 v[2:3], s[58:59], v[108:109], v[2:3] op_sel:[1,0,0]
	v_pk_fma_f32 v[4:5], s[58:59], v[110:111], v[4:5] op_sel:[1,0,0]
	s_waitcnt vmcnt(11)
	v_pk_fma_f32 v[14:15], s[36:37], v[112:113], v[14:15] op_sel_hi:[0,1,1]
	v_pk_fma_f32 v[16:17], s[36:37], v[114:115], v[16:17] op_sel_hi:[0,1,1]
	v_pk_fma_f32 v[10:11], s[44:45], v[112:113], v[10:11] op_sel_hi:[0,1,1]
	v_pk_fma_f32 v[12:13], s[44:45], v[114:115], v[12:13] op_sel_hi:[0,1,1]
	v_pk_fma_f32 v[6:7], s[52:53], v[112:113], v[6:7] op_sel_hi:[0,1,1]
	v_pk_fma_f32 v[8:9], s[52:53], v[114:115], v[8:9] op_sel_hi:[0,1,1]
	v_pk_fma_f32 v[2:3], s[60:61], v[112:113], v[2:3] op_sel_hi:[0,1,1]
	v_pk_fma_f32 v[4:5], s[60:61], v[114:115], v[4:5] op_sel_hi:[0,1,1]
	s_waitcnt vmcnt(10)
	v_pk_fma_f32 v[14:15], s[36:37], v[116:117], v[14:15] op_sel:[1,0,0]
	v_pk_fma_f32 v[16:17], s[36:37], v[118:119], v[16:17] op_sel:[1,0,0]
	v_pk_fma_f32 v[10:11], s[44:45], v[116:117], v[10:11] op_sel:[1,0,0]
	v_pk_fma_f32 v[12:13], s[44:45], v[118:119], v[12:13] op_sel:[1,0,0]
	v_pk_fma_f32 v[6:7], s[52:53], v[116:117], v[6:7] op_sel:[1,0,0]
	v_pk_fma_f32 v[8:9], s[52:53], v[118:119], v[8:9] op_sel:[1,0,0]
	v_pk_fma_f32 v[2:3], s[60:61], v[116:117], v[2:3] op_sel:[1,0,0]
	v_pk_fma_f32 v[4:5], s[60:61], v[118:119], v[4:5] op_sel:[1,0,0]
	s_waitcnt vmcnt(9)
	v_pk_fma_f32 v[14:15], s[38:39], v[120:121], v[14:15] op_sel_hi:[0,1,1]
	v_pk_fma_f32 v[16:17], s[38:39], v[122:123], v[16:17] op_sel_hi:[0,1,1]
	v_pk_fma_f32 v[10:11], s[46:47], v[120:121], v[10:11] op_sel_hi:[0,1,1]
	v_pk_fma_f32 v[12:13], s[46:47], v[122:123], v[12:13] op_sel_hi:[0,1,1]
	v_pk_fma_f32 v[6:7], s[54:55], v[120:121], v[6:7] op_sel_hi:[0,1,1]
	v_pk_fma_f32 v[8:9], s[54:55], v[122:123], v[8:9] op_sel_hi:[0,1,1]
	v_pk_fma_f32 v[2:3], s[62:63], v[120:121], v[2:3] op_sel_hi:[0,1,1]
	v_pk_fma_f32 v[4:5], s[62:63], v[122:123], v[4:5] op_sel_hi:[0,1,1]
	s_waitcnt vmcnt(8)
	v_pk_fma_f32 v[14:15], s[38:39], v[124:125], v[14:15] op_sel:[1,0,0]
	v_pk_fma_f32 v[16:17], s[38:39], v[126:127], v[16:17] op_sel:[1,0,0]
	v_pk_fma_f32 v[10:11], s[46:47], v[124:125], v[10:11] op_sel:[1,0,0]
	v_pk_fma_f32 v[12:13], s[46:47], v[126:127], v[12:13] op_sel:[1,0,0]
	v_pk_fma_f32 v[6:7], s[54:55], v[124:125], v[6:7] op_sel:[1,0,0]
	v_pk_fma_f32 v[8:9], s[54:55], v[126:127], v[8:9] op_sel:[1,0,0]
	v_pk_fma_f32 v[2:3], s[62:63], v[124:125], v[2:3] op_sel:[1,0,0]
	v_pk_fma_f32 v[4:5], s[62:63], v[126:127], v[4:5] op_sel:[1,0,0]
	s_waitcnt lgkmcnt(0)
	s_waitcnt vmcnt(7)
	v_pk_fma_f32 v[14:15], s[64:65], v[128:129], v[14:15] op_sel_hi:[0,1,1]
	v_pk_fma_f32 v[16:17], s[64:65], v[130:131], v[16:17] op_sel_hi:[0,1,1]
	v_pk_fma_f32 v[10:11], s[72:73], v[128:129], v[10:11] op_sel_hi:[0,1,1]
	v_pk_fma_f32 v[12:13], s[72:73], v[130:131], v[12:13] op_sel_hi:[0,1,1]
	v_pk_fma_f32 v[6:7], s[80:81], v[128:129], v[6:7] op_sel_hi:[0,1,1]
	v_pk_fma_f32 v[8:9], s[80:81], v[130:131], v[8:9] op_sel_hi:[0,1,1]
	v_pk_fma_f32 v[2:3], s[88:89], v[128:129], v[2:3] op_sel_hi:[0,1,1]
	v_pk_fma_f32 v[4:5], s[88:89], v[130:131], v[4:5] op_sel_hi:[0,1,1]
	s_waitcnt vmcnt(6)
	v_pk_fma_f32 v[14:15], s[64:65], v[132:133], v[14:15] op_sel:[1,0,0]
	v_pk_fma_f32 v[16:17], s[64:65], v[134:135], v[16:17] op_sel:[1,0,0]
	v_pk_fma_f32 v[10:11], s[72:73], v[132:133], v[10:11] op_sel:[1,0,0]
	v_pk_fma_f32 v[12:13], s[72:73], v[134:135], v[12:13] op_sel:[1,0,0]
	v_pk_fma_f32 v[6:7], s[80:81], v[132:133], v[6:7] op_sel:[1,0,0]
	v_pk_fma_f32 v[8:9], s[80:81], v[134:135], v[8:9] op_sel:[1,0,0]
	v_pk_fma_f32 v[2:3], s[88:89], v[132:133], v[2:3] op_sel:[1,0,0]
	v_pk_fma_f32 v[4:5], s[88:89], v[134:135], v[4:5] op_sel:[1,0,0]
	s_waitcnt vmcnt(5)
	v_pk_fma_f32 v[14:15], s[66:67], v[136:137], v[14:15] op_sel_hi:[0,1,1]
	v_pk_fma_f32 v[16:17], s[66:67], v[138:139], v[16:17] op_sel_hi:[0,1,1]
	v_pk_fma_f32 v[10:11], s[74:75], v[136:137], v[10:11] op_sel_hi:[0,1,1]
	v_pk_fma_f32 v[12:13], s[74:75], v[138:139], v[12:13] op_sel_hi:[0,1,1]
	v_pk_fma_f32 v[6:7], s[82:83], v[136:137], v[6:7] op_sel_hi:[0,1,1]
	v_pk_fma_f32 v[8:9], s[82:83], v[138:139], v[8:9] op_sel_hi:[0,1,1]
	v_pk_fma_f32 v[2:3], s[90:91], v[136:137], v[2:3] op_sel_hi:[0,1,1]
	v_pk_fma_f32 v[4:5], s[90:91], v[138:139], v[4:5] op_sel_hi:[0,1,1]
	s_waitcnt vmcnt(4)
	v_pk_fma_f32 v[14:15], s[66:67], v[140:141], v[14:15] op_sel:[1,0,0]
	v_pk_fma_f32 v[16:17], s[66:67], v[142:143], v[16:17] op_sel:[1,0,0]
	v_pk_fma_f32 v[10:11], s[74:75], v[140:141], v[10:11] op_sel:[1,0,0]
	v_pk_fma_f32 v[12:13], s[74:75], v[142:143], v[12:13] op_sel:[1,0,0]
	v_pk_fma_f32 v[6:7], s[82:83], v[140:141], v[6:7] op_sel:[1,0,0]
	v_pk_fma_f32 v[8:9], s[82:83], v[142:143], v[8:9] op_sel:[1,0,0]
	v_pk_fma_f32 v[2:3], s[90:91], v[140:141], v[2:3] op_sel:[1,0,0]
	v_pk_fma_f32 v[4:5], s[90:91], v[142:143], v[4:5] op_sel:[1,0,0]
	s_waitcnt vmcnt(3)
	v_pk_fma_f32 v[14:15], s[68:69], v[144:145], v[14:15] op_sel_hi:[0,1,1]
	v_pk_fma_f32 v[16:17], s[68:69], v[146:147], v[16:17] op_sel_hi:[0,1,1]
	v_pk_fma_f32 v[10:11], s[76:77], v[144:145], v[10:11] op_sel_hi:[0,1,1]
	v_pk_fma_f32 v[12:13], s[76:77], v[146:147], v[12:13] op_sel_hi:[0,1,1]
	v_pk_fma_f32 v[6:7], s[84:85], v[144:145], v[6:7] op_sel_hi:[0,1,1]
	v_pk_fma_f32 v[8:9], s[84:85], v[146:147], v[8:9] op_sel_hi:[0,1,1]
	v_pk_fma_f32 v[2:3], s[92:93], v[144:145], v[2:3] op_sel_hi:[0,1,1]
	v_pk_fma_f32 v[4:5], s[92:93], v[146:147], v[4:5] op_sel_hi:[0,1,1]
	s_waitcnt vmcnt(2)
	v_pk_fma_f32 v[14:15], s[68:69], v[148:149], v[14:15] op_sel:[1,0,0]
	v_pk_fma_f32 v[16:17], s[68:69], v[150:151], v[16:17] op_sel:[1,0,0]
	v_pk_fma_f32 v[10:11], s[76:77], v[148:149], v[10:11] op_sel:[1,0,0]
	v_pk_fma_f32 v[12:13], s[76:77], v[150:151], v[12:13] op_sel:[1,0,0]
	v_pk_fma_f32 v[6:7], s[84:85], v[148:149], v[6:7] op_sel:[1,0,0]
	v_pk_fma_f32 v[8:9], s[84:85], v[150:151], v[8:9] op_sel:[1,0,0]
	v_pk_fma_f32 v[2:3], s[92:93], v[148:149], v[2:3] op_sel:[1,0,0]
	v_pk_fma_f32 v[4:5], s[92:93], v[150:151], v[4:5] op_sel:[1,0,0]
	s_waitcnt vmcnt(1)
	v_pk_fma_f32 v[14:15], s[70:71], v[152:153], v[14:15] op_sel_hi:[0,1,1]
	v_pk_fma_f32 v[16:17], s[70:71], v[154:155], v[16:17] op_sel_hi:[0,1,1]
	v_pk_fma_f32 v[10:11], s[78:79], v[152:153], v[10:11] op_sel_hi:[0,1,1]
	v_pk_fma_f32 v[12:13], s[78:79], v[154:155], v[12:13] op_sel_hi:[0,1,1]
	v_pk_fma_f32 v[6:7], s[86:87], v[152:153], v[6:7] op_sel_hi:[0,1,1]
	v_pk_fma_f32 v[8:9], s[86:87], v[154:155], v[8:9] op_sel_hi:[0,1,1]
	v_pk_fma_f32 v[2:3], s[94:95], v[152:153], v[2:3] op_sel_hi:[0,1,1]
	v_pk_fma_f32 v[4:5], s[94:95], v[154:155], v[4:5] op_sel_hi:[0,1,1]
	s_waitcnt vmcnt(0)
	v_pk_fma_f32 v[14:15], s[70:71], v[156:157], v[14:15] op_sel:[1,0,0]
	v_pk_fma_f32 v[16:17], s[70:71], v[158:159], v[16:17] op_sel:[1,0,0]
	v_pk_fma_f32 v[10:11], s[78:79], v[156:157], v[10:11] op_sel:[1,0,0]
	v_pk_fma_f32 v[12:13], s[78:79], v[158:159], v[12:13] op_sel:[1,0,0]
	v_pk_fma_f32 v[6:7], s[86:87], v[156:157], v[6:7] op_sel:[1,0,0]
	v_pk_fma_f32 v[8:9], s[86:87], v[158:159], v[8:9] op_sel:[1,0,0]
	v_pk_fma_f32 v[2:3], s[94:95], v[156:157], v[2:3] op_sel:[1,0,0]
	v_pk_fma_f32 v[4:5], s[94:95], v[158:159], v[4:5] op_sel:[1,0,0]
	s_cmp_eq_u32 s22, 0
	s_cselect_b64 s[4:5], -1, 0
	s_and_b64 vcc, exec, s[4:5]
	s_cbranch_vccnz .LBB0_5
	v_lshl_or_b32 v1, s22, 13, v26
	v_add_u32_e32 v18, 0xffffe000, v1
	ds_write_b128 v18, v[14:17]
	v_add_u32_e32 v18, 0xffffe800, v1
	ds_write_b128 v18, v[10:13]
	v_add_u32_e32 v18, 0xfffff000, v1
	v_add_u32_e32 v1, 0xfffff800, v1
	ds_write_b128 v18, v[6:9]
	ds_write_b128 v1, v[2:5]
.LBB0_5:
	s_andn2_b64 vcc, exec, s[4:5]
	s_waitcnt lgkmcnt(0)
	s_barrier
	s_cbranch_vccnz .LBB0_7
	s_mov_b64 s[4:5], s[28:29]
	ds_read_b128 v[18:21], v26
	ds_read_b128 v[22:25], v26 offset:8192
	ds_read_b128 v[28:31], v26 offset:16384
	ds_read_b128 v[32:35], v26 offset:2048
	ds_read_b128 v[36:39], v26 offset:10240
	v_mov_b32_e32 v27, 0
	ds_read_b128 v[40:43], v26 offset:18432
	s_mov_b32 s7, 0
	s_lshl_b32 s6, s3, 9
	s_waitcnt lgkmcnt(0)
	v_lshl_add_u64 v[44:45], s[4:5], 0, v[26:27]
	v_pk_add_f32 v[14:15], v[14:15], v[18:19]
	v_pk_add_f32 v[16:17], v[16:17], v[20:21]
	v_lshl_add_u64 v[46:47], s[6:7], 2, v[44:45]
	v_pk_add_f32 v[14:15], v[14:15], v[22:23]
	v_pk_add_f32 v[16:17], v[16:17], v[24:25]
	s_lshl_b32 s6, s2, 11
	v_pk_add_f32 v[14:15], v[14:15], v[28:29]
	v_pk_add_f32 v[16:17], v[16:17], v[30:31]
	v_lshl_add_u64 v[44:45], s[6:7], 2, v[44:45]
	v_pk_add_f32 v[10:11], v[10:11], v[32:33]
	v_pk_add_f32 v[12:13], v[12:13], v[34:35]
	s_mov_b32 s3, 0xfff81000
	global_store_dwordx4 v[46:47], v[14:17], off
	ds_read_b128 v[14:17], v26 offset:4096
	v_pk_add_f32 v[10:11], v[10:11], v[36:37]
	v_pk_add_f32 v[12:13], v[12:13], v[38:39]
	v_add_co_u32_e32 v36, vcc, s3, v44
	v_pk_add_f32 v[10:11], v[10:11], v[40:41]
	v_pk_add_f32 v[12:13], v[12:13], v[42:43]
	v_addc_co_u32_e32 v37, vcc, -1, v45, vcc
	global_store_dwordx4 v[36:37], v[10:13], off offset:-2048
	ds_read_b128 v[10:13], v26 offset:12288
	ds_read_b128 v[18:21], v26 offset:20480
	ds_read_b128 v[22:25], v26 offset:6144
	ds_read_b128 v[28:31], v26 offset:14336
	ds_read_b128 v[32:35], v26 offset:22528
	s_waitcnt lgkmcnt(5)
	v_pk_add_f32 v[6:7], v[6:7], v[14:15]
	v_pk_add_f32 v[8:9], v[8:9], v[16:17]
	s_waitcnt lgkmcnt(4)
	v_pk_add_f32 v[6:7], v[6:7], v[10:11]
	v_pk_add_f32 v[8:9], v[8:9], v[12:13]
	s_waitcnt lgkmcnt(3)
	v_pk_add_f32 v[6:7], v[6:7], v[18:19]
	v_pk_add_f32 v[8:9], v[8:9], v[20:21]
	s_waitcnt lgkmcnt(2)
	v_pk_add_f32 v[2:3], v[2:3], v[22:23]
	v_pk_add_f32 v[4:5], v[4:5], v[24:25]
	global_store_dwordx4 v[36:37], v[6:9], off
	s_waitcnt lgkmcnt(1)
	v_pk_add_f32 v[2:3], v[2:3], v[28:29]
	v_pk_add_f32 v[4:5], v[4:5], v[30:31]
	v_add_co_u32_e32 v6, vcc, 0xfff82000, v44
	s_waitcnt lgkmcnt(0)
	v_pk_add_f32 v[2:3], v[2:3], v[32:33]
	v_pk_add_f32 v[4:5], v[4:5], v[34:35]
	v_addc_co_u32_e32 v7, vcc, -1, v45, vcc
	global_store_dwordx4 v[6:7], v[2:5], off offset:-2048
